# baseline (speedup 1.0000x reference)
.LBB2_29:
	s_waitcnt vmcnt(2)
	v_add_f32_e32 v2, 0x24e69595, v106
	v_rcp_f32_e32 v2, v2
	s_waitcnt vmcnt(0)
	v_lshlrev_b32_e32 v60, 10, v73
	v_bitop3_b32 v61, v62, v73, 15 bitop3:0x78
	v_lshl_or_b32 v61, v61, 4, v60
	v_cndmask_b32_e64 v2, 0, v2, s[8:9]
	v_cvt_f16_f32_e32 v3, v2
	v_fma_mixlo_f16 v2, v2, v77, 0
	v_and_b32_e32 v55, 15, v73
	s_add_i32 s6, s15, 0x200
	v_pk_mul_f16 v4, v3, v109 op_sel_hi:[0,1]
	v_pk_fma_f16 v56, v50, v2, v4 op_sel_hi:[1,0,1]
	v_add_f32_e32 v4, 0x24e69595, v102
	v_pk_mul_f16 v5, v3, v108 op_sel_hi:[0,1]
	v_pk_mul_f16 v6, v3, v107 op_sel_hi:[0,1]
	v_rcp_f32_e32 v4, v4
	v_pk_mul_f16 v3, v3, v105 op_sel_hi:[0,1]
	v_pk_fma_f16 v57, v51, v2, v5 op_sel_hi:[1,0,1]
	v_pk_fma_f16 v58, v52, v2, v6 op_sel_hi:[1,0,1]
	v_pk_fma_f16 v59, v53, v2, v3 op_sel_hi:[1,0,1]
	v_lshrrev_b32_e32 v2, 1, v71
	v_and_b32_e32 v2, 16, v2
	v_lshl_or_b32 v14, v69, 7, v2
	v_cndmask_b32_e64 v64, 0, v4, s[8:9]
	global_load_dwordx4 v[2:5], v14, s[36:37]
	global_load_dwordx4 v[6:9], v14, s[36:37] offset:32
	global_load_dwordx4 v[10:13], v14, s[36:37] offset:64
	s_nop 0
	global_load_dwordx4 v[14:17], v14, s[36:37] offset:96
	v_cvt_f16_f32_e32 v77, v64
	ds_write_b128 v61, v[56:59]
	v_add_f32_e32 v61, 0x24e69595, v83
	v_rcp_f32_e32 v61, v61
	v_fma_mixlo_f16 v59, v64, v78, 0
	v_pk_mul_f16 v56, v77, v97 op_sel_hi:[0,1]
	v_pk_mul_f16 v57, v77, v95 op_sel_hi:[0,1]
	v_pk_mul_f16 v58, v77, v94 op_sel_hi:[0,1]
	v_pk_mul_f16 v64, v77, v92 op_sel_hi:[0,1]
	v_pk_fma_f16 v56, v50, v59, v56 op_sel_hi:[1,0,1]
	v_pk_fma_f16 v57, v51, v59, v57 op_sel_hi:[1,0,1]
	v_pk_fma_f16 v58, v52, v59, v58 op_sel_hi:[1,0,1]
	v_pk_fma_f16 v59, v53, v59, v64 op_sel_hi:[1,0,1]
	v_bitop3_b32 v64, v74, v73, 15 bitop3:0x78
	v_cndmask_b32_e64 v61, 0, v61, s[8:9]
	v_lshl_add_u32 v64, v64, 4, v60
	v_cvt_f16_f32_e32 v73, v61
	ds_write_b128 v64, v[56:59]
	v_fma_mixlo_f16 v59, v61, v76, 0
	v_add_f32_e32 v61, 0x24e69595, v80
	v_rcp_f32_e32 v61, v61
	v_pk_mul_f16 v56, v73, v90 op_sel_hi:[0,1]
	v_pk_mul_f16 v57, v73, v89 op_sel_hi:[0,1]
	v_pk_mul_f16 v58, v73, v88 op_sel_hi:[0,1]
	v_cndmask_b32_e64 v61, 0, v61, s[8:9]
	v_pk_mul_f16 v64, v73, v87 op_sel_hi:[0,1]
	v_cvt_f16_f32_e32 v73, v61
	v_pk_fma_f16 v56, v50, v59, v56 op_sel_hi:[1,0,1]
	v_pk_fma_f16 v57, v51, v59, v57 op_sel_hi:[1,0,1]
	v_pk_fma_f16 v58, v52, v59, v58 op_sel_hi:[1,0,1]
	v_pk_fma_f16 v59, v53, v59, v64 op_sel_hi:[1,0,1]
	v_bitop3_b32 v64, v62, v55, 32 bitop3:0x36
	v_lshl_or_b32 v64, v64, 4, v60
	ds_write_b128 v64, v[56:59]
	v_fma_mixlo_f16 v56, v61, v75, 0
	v_pk_mul_f16 v57, v73, v85 op_sel_hi:[0,1]
	v_pk_fma_f16 v50, v50, v56, v57 op_sel_hi:[1,0,1]
	v_pk_mul_f16 v57, v73, v84 op_sel_hi:[0,1]
	v_pk_fma_f16 v51, v51, v56, v57 op_sel_hi:[1,0,1]
	v_pk_mul_f16 v57, v73, v82 op_sel_hi:[0,1]
	v_pk_fma_f16 v52, v52, v56, v57 op_sel_hi:[1,0,1]
	v_pk_mul_f16 v57, v73, v81 op_sel_hi:[0,1]
	v_bitop3_b32 v55, v62, v55, 48 bitop3:0x36
	v_pk_fma_f16 v53, v53, v56, v57 op_sel_hi:[1,0,1]
	v_lshl_or_b32 v55, v55, 4, v60
	ds_write_b128 v55, v[50:53]
	v_lshl_add_u32 v50, s6, 5, v70
	v_or_b32_e32 v55, v50, v68
	v_cmp_gt_i32_e32 vcc, s3, v55
	v_and_b32_e32 v54, 63, v71
	v_and_b32_e32 v75, 31, v71
	v_cndmask_b32_e32 v57, v65, v55, vcc
	v_lshlrev_b32_e32 v50, 2, v57
	v_lshlrev_b32_e32 v73, 5, v57
	global_load_dword v56, v50, s[12:13]
	v_or_b32_e32 v50, v73, v62
	v_lshlrev_b32_e32 v50, 2, v50
	global_load_dword v64, v50, s[28:29]
	v_ashrrev_i32_e32 v50, 4, v71
	v_and_b32_e32 v74, -16, v50
	v_add_u32_e32 v50, s22, v74
	v_or_b32_e32 v50, v50, v62
	v_min_i32_e32 v50, 0xc34f, v50
	v_lshlrev_b32_e32 v50, 2, v50
	global_load_dword v78, v50, s[12:13]
	v_ashrrev_i32_e32 v50, 3, v71
	v_and_b32_e32 v58, -16, v50
	v_lshrrev_b32_e32 v54, 5, v54
	v_lshlrev_b32_e32 v76, 10, v75
	v_bitop3_b32 v50, v58, v62, v54 bitop3:0x36
	v_lshl_add_u32 v50, v50, 4, v76
	s_waitcnt lgkmcnt(0)
	s_barrier
	s_setprio 3
	ds_read_b128 v[50:53], v50
	v_or_b32_e32 v54, v58, v54
	v_bitop3_b32 v58, v54, v62, 2 bitop3:0x36
	v_lshl_add_u32 v58, v58, 4, v76
	ds_read_b128 v[58:61], v58
	s_waitcnt vmcnt(3) lgkmcnt(1)
	v_mfma_f32_32x32x16_f16 v[2:17], v[18:21], v[50:53], v[2:17]
	v_bitop3_b32 v50, v54, v62, 4 bitop3:0x36
	v_lshl_add_u32 v50, v50, 4, v76
	ds_read_b128 v[50:53], v50
	v_lshrrev_b32_e32 v71, 2, v71
	s_waitcnt vmcnt(2)
	v_cmp_gt_i32_e64 s[4:5], v56, v62
	s_waitcnt lgkmcnt(1)
	v_mfma_f32_32x32x16_f16 v[2:17], v[22:25], v[58:61], v[2:17]
	v_bitop3_b32 v58, v54, v62, 6 bitop3:0x36
	v_lshl_add_u32 v58, v58, 4, v76
	ds_read_b128 v[58:61], v58
	s_waitcnt lgkmcnt(1)
	v_mfma_f32_32x32x16_f16 v[2:17], v[26:29], v[50:53], v[2:17]
	v_bitop3_b32 v50, v54, v62, 8 bitop3:0x36
	v_lshl_add_u32 v50, v50, 4, v76
	ds_read_b128 v[50:53], v50
	s_waitcnt lgkmcnt(1)
	v_mfma_f32_32x32x16_f16 v[2:17], v[30:33], v[58:61], v[2:17]
	v_bitop3_b32 v58, v54, v62, 10 bitop3:0x36
	v_lshl_add_u32 v58, v58, 4, v76
	ds_read_b128 v[58:61], v58
	s_waitcnt lgkmcnt(1)
	v_mfma_f32_32x32x16_f16 v[2:17], v[34:37], v[50:53], v[2:17]
	v_bitop3_b32 v50, v54, v62, 12 bitop3:0x36
	v_lshl_add_u32 v50, v50, 4, v76
	ds_read_b128 v[50:53], v50
	v_bitop3_b32 v54, v54, v62, 14 bitop3:0x36
	v_lshl_add_u32 v54, v54, 4, v76
	s_waitcnt lgkmcnt(1)
	v_mfma_f32_32x32x16_f16 v[2:17], v[38:41], v[58:61], v[2:17]
	ds_read_b128 v[58:61], v54
	v_or_b32_e32 v54, v74, v62
	s_waitcnt lgkmcnt(1)
	v_mfma_f32_32x32x16_f16 v[2:17], v[42:45], v[50:53], v[2:17]
	v_lshlrev_b32_e32 v52, 9, v75
	v_sub_u32_e32 v52, v76, v52
	v_xor_b32_e32 v50, v70, v62
	v_and_or_b32 v52, v71, 8, v52
	v_bitop3_b32 v51, v70, v62, 1 bitop3:0x36
	v_lshl_add_u32 v50, v50, 4, v52
	v_lshl_add_u32 v51, v51, 4, v52
	s_waitcnt lgkmcnt(0)
	v_mfma_f32_32x32x16_f16 v[2:17], v[46:49], v[58:61], v[2:17]
	s_nop 11
	v_cvt_pk_f16_f32 v2, v2, v3
	v_cvt_pk_f16_f32 v3, v4, v5
	v_cvt_pk_f16_f32 v4, v6, v7
	v_cvt_pk_f16_f32 v5, v8, v9
	v_pk_max_f16 v2, v2, 0
	v_pk_max_f16 v3, v3, 0
	v_pk_max_f16 v4, v4, 0
	v_pk_max_f16 v5, v5, 0
	ds_write_b64 v50, v[2:3] offset:32768
	ds_write_b64 v51, v[4:5] offset:32768
	v_cvt_pk_f16_f32 v2, v10, v11
	v_cvt_pk_f16_f32 v3, v12, v13
	v_bitop3_b32 v4, v70, v62, 2 bitop3:0x36
	v_pk_max_f16 v2, v2, 0
	v_pk_max_f16 v3, v3, 0
	v_lshl_add_u32 v4, v4, 4, v52
	ds_write_b64 v4, v[2:3] offset:32768
	v_cvt_pk_f16_f32 v2, v14, v15
	v_cvt_pk_f16_f32 v3, v16, v17
	v_bitop3_b32 v4, v70, v62, 3 bitop3:0x36
	v_pk_max_f16 v2, v2, 0
	v_pk_max_f16 v3, v3, 0
	v_lshl_add_u32 v4, v4, 4, v52
	ds_write_b64 v4, v[2:3] offset:32768
	s_waitcnt vmcnt(1)
	v_cndmask_b32_e64 v2, v55, v64, s[4:5]
	v_cndmask_b32_e32 v64, v65, v2, vcc
	v_lshlrev_b32_e32 v2, 5, v64
	s_waitcnt lgkmcnt(0)
	s_barrier
	global_load_dwordx4 v[6:9], v2, s[18:19]
	s_nop 0
	global_load_dwordx4 v[2:5], v73, s[18:19] offset:16
	global_load_dwordx4 v[10:13], v73, s[18:19]
	v_lshl_or_b32 v14, v57, 8, v72
	global_load_dwordx4 v[50:53], v14, s[16:17]
	v_lshlrev_b32_e32 v14, 4, v69
	v_and_b32_e32 v57, 48, v14
	v_or_b32_e32 v14, v57, v62
	v_lshlrev_b32_e32 v55, 9, v14
	v_xor_b32_e32 v14, v68, v62
	v_lshlrev_b32_e32 v58, 4, v14
	v_or_b32_e32 v14, v55, v58
	ds_read_b128 v[14:17], v14 offset:49152
	v_lshlrev_b32_e32 v69, 9, v54
	v_or_b32_e32 v58, v69, v58
	v_bitop3_b32 v70, v68, v62, 4 bitop3:0x36
	ds_read_b128 v[58:61], v58 offset:32768
	v_lshlrev_b32_e32 v74, 4, v70
	v_or_b32_e32 v70, v55, v74
	ds_read_b128 v[70:73], v70 offset:49152
	s_waitcnt lgkmcnt(1)
	v_mfma_f32_16x16x32_f16 v[14:17], v[14:17], v[58:61], 0
	v_or_b32_e32 v58, v69, v74
	v_bitop3_b32 v74, v68, v62, 8 bitop3:0x36
	ds_read_b128 v[58:61], v58 offset:32768
	v_lshlrev_b32_e32 v79, 4, v74
	v_or_b32_e32 v74, v55, v79
	ds_read_b128 v[74:77], v74 offset:49152
	s_waitcnt lgkmcnt(1)
	v_mfma_f32_16x16x32_f16 v[14:17], v[70:73], v[58:61], v[14:17]
	v_or_b32_e32 v58, v69, v79
	v_bitop3_b32 v70, v68, v62, 12 bitop3:0x36
	ds_read_b128 v[58:61], v58 offset:32768
	v_lshlrev_b32_e32 v79, 4, v70
	v_or_b32_e32 v70, v55, v79
	ds_read_b128 v[70:73], v70 offset:49152
	s_waitcnt lgkmcnt(1)
	v_mfma_f32_16x16x32_f16 v[14:17], v[74:77], v[58:61], v[14:17]
	v_or_b32_e32 v58, v69, v79
	v_bitop3_b32 v74, v68, v62, 16 bitop3:0x36
	ds_read_b128 v[58:61], v58 offset:32768
	v_lshlrev_b32_e32 v79, 4, v74
	v_or_b32_e32 v74, v55, v79
	ds_read_b128 v[74:77], v74 offset:49152
	s_waitcnt lgkmcnt(1)
	v_mfma_f32_16x16x32_f16 v[14:17], v[70:73], v[58:61], v[14:17]
	v_or_b32_e32 v58, v69, v79
	v_bitop3_b32 v70, v68, v62, 20 bitop3:0x36
	ds_read_b128 v[58:61], v58 offset:32768
	v_lshlrev_b32_e32 v79, 4, v70
	v_or_b32_e32 v70, v55, v79
	ds_read_b128 v[70:73], v70 offset:49152
	s_waitcnt lgkmcnt(1)
	v_mfma_f32_16x16x32_f16 v[14:17], v[74:77], v[58:61], v[14:17]
	v_or_b32_e32 v58, v69, v79
	v_bitop3_b32 v74, v68, v62, 24 bitop3:0x36
	ds_read_b128 v[58:61], v58 offset:32768
	v_lshlrev_b32_e32 v79, 4, v74
	v_or_b32_e32 v74, v55, v79
	ds_read_b128 v[74:77], v74 offset:49152
	v_bitop3_b32 v62, v68, v62, 28 bitop3:0x36
	s_waitcnt lgkmcnt(1)
	v_mfma_f32_16x16x32_f16 v[14:17], v[70:73], v[58:61], v[14:17]
	v_or_b32_e32 v58, v69, v79
	v_lshlrev_b32_e32 v62, 4, v62
	ds_read_b128 v[58:61], v58 offset:32768
	v_or_b32_e32 v55, v55, v62
	ds_read_b128 v[70:73], v55 offset:49152
	v_or_b32_e32 v55, v69, v62
	s_waitcnt lgkmcnt(1)
	v_mfma_f32_16x16x32_f16 v[14:17], v[74:77], v[58:61], v[14:17]
	ds_read_b128 v[58:61], v55 offset:32768
	v_add_u32_e32 v54, s22, v54
	v_cmp_gt_i32_e32 vcc, s3, v54
	s_waitcnt lgkmcnt(0)
	v_mfma_f32_16x16x32_f16 v[14:17], v[70:73], v[58:61], v[14:17]
	s_waitcnt vmcnt(4)
	v_cmp_gt_i32_e64 s[4:5], 33, v78
	s_and_b64 s[8:9], vcc, s[4:5]
	s_and_saveexec_b64 s[4:5], s[8:9]
	s_cbranch_execz .LBB2_2
	v_ashrrev_i32_e32 v55, 31, v54
	s_nop 1
	v_cvt_pk_f16_f32 v17, v16, v17
	v_cvt_pk_f16_f32 v16, v14, v15
	v_lshlrev_b64 v[14:15], 7, v[54:55]
	v_lshlrev_b32_e32 v1, 1, v57
	v_lshl_add_u64 v[14:15], s[10:11], 0, v[14:15]
	v_lshl_or_b32 v62, v68, 3, v1
	v_lshl_add_u64 v[14:15], v[14:15], 0, v[62:63]
	global_store_dwordx2 v[14:15], v[16:17], off
	s_branch .LBB2_2
